# grid-size guard: any grid other than 256 workgroups takes the original phase-12 path; otherwise identical to the scalar-index version
# baseline (speedup 1.0000x reference)
.LBB0_1463:
	s_load_dword s25, s[0:1], 0xd8
	s_waitcnt lgkmcnt(0)
	s_cmp_lg_u32 s25, 0x100
	s_cbranch_scc1 .Lpeer_orig
	s_mov_b64 exec, -1
	s_mov_b32 s55, 0
	s_waitcnt vmcnt(0)
	v_cmp_eq_u32_e32 vcc, 0, v0
	s_waitcnt vmcnt(0) lgkmcnt(0)
	s_barrier
	s_and_saveexec_b64 s[2:3], vcc
	s_cbranch_execz .Lgba_1444
	v_readlane_b32 s4, v237, 5
	s_waitcnt vmcnt(0) expcnt(0) lgkmcnt(0)
	s_nop 0
	v_mov_b32_e32 v1, s4
	ds_read_b32 v3, v1
	ds_read_b32 v1, v1 offset:4
	s_waitcnt lgkmcnt(1)
	v_cmp_ne_u32_e32 vcc, 0, v3
	s_branch .Lgba_1412
	v_readlane_b32 s4, v237, 2
	v_readlane_b32 s5, v237, 3
	s_load_dwordx2 s[8:9], s[6:7], 0x4
	s_lshl_b64 s[4:5], s[4:5], 2
	v_readlane_b32 s6, v237, 0
	s_add_u32 s4, s6, s4
	v_readlane_b32 s6, v237, 1
	s_addc_u32 s5, s6, s5
	s_add_u32 s6, s4, 0x1000
	s_addc_u32 s7, s5, 0
	s_waitcnt lgkmcnt(0)
	s_mul_i32 s20, s8, s38
	s_add_u32 s8, s4, 0x1100
	s_mul_i32 s20, s20, s9
	s_addc_u32 s9, s5, 0
	s_add_u32 s10, s4, 0x1200
	s_addc_u32 s11, s5, 0
	s_add_u32 s12, s4, 0x1300
	s_addc_u32 s13, s5, 0
	s_mov_b32 s21, 1
	v_mov_b32_e32 v17, 0
	s_branch .Lgba_1400
